# LDS bank conflicts: router phase (layer 0) weight tables XOR-swizzled (16-byte chunk index ^ column) in writer and ds_read_b128 reader
# baseline (speedup 1.0000x reference)
.LBB0_899:
	global_load_dword v23, v[26:27], off
	global_load_dwordx4 v[10:13], v[28:29], off
	global_load_dwordx4 v[18:21], v[24:25], off offset:-32
	global_load_dwordx4 v[14:17], v[24:25], off offset:-16
	global_load_dwordx4 v[6:9], v[24:25], off
	global_load_dwordx4 v[2:5], v[24:25], off offset:16
	v_add_co_u32_e32 v1, vcc, 0x200, v1
	s_xor_b64 s[14:15], vcc, -1
	s_and_b64 s[14:15], exec, s[14:15]
	v_xor_b32_e32 v100, 16, v30
	v_xor_b32_e32 v101, 32, v30
	v_xor_b32_e32 v102, 48, v30
	v_xor_b32_e32 v103, 64, v30
	v_xor_b32_e32 v104, 0x50, v30
	v_xor_b32_e32 v105, 0x60, v30
	v_xor_b32_e32 v106, 0x70, v30
	v_xor_b32_e32 v107, 0x80, v30
	v_xor_b32_e32 v108, 0x90, v30
	v_xor_b32_e32 v109, 0xa0, v30
	v_xor_b32_e32 v110, 0xb0, v30
	v_xor_b32_e32 v111, 0xc0, v30
	v_xor_b32_e32 v112, 0xd0, v30
	v_xor_b32_e32 v113, 0xe0, v30
	v_xor_b32_e32 v114, 0xf0, v30
	v_add_u32_e32 v31, 0x10000, v111
	v_add_u32_e32 v32, 0x10800, v112
	v_add_u32_e32 v33, 0x11000, v113
	v_add_u32_e32 v34, 0x11800, v114
	v_add_u32_e32 v35, 0x12000, v30
	v_add_u32_e32 v36, 0x12800, v100
	v_add_u32_e32 v37, 0x13000, v101
	v_add_u32_e32 v38, 0x13800, v102
	v_lshl_add_u64 v[24:25], v[24:25], 0, s[6:7]
	v_lshl_add_u64 v[26:27], v[26:27], 0, s[8:9]
	v_lshl_add_u64 v[28:29], v[28:29], 0, s[10:11]
	s_or_b64 s[4:5], s[14:15], s[4:5]
	s_waitcnt vmcnt(4)
	v_mul_f32_e32 v39, v23, v10
	v_mul_f32_e32 v40, v23, v11
	v_mul_f32_e32 v41, v23, v12
	v_mul_f32_e32 v42, v23, v13
	s_waitcnt vmcnt(3)
	v_mul_f32_e32 v43, v23, v18
	v_mul_f32_e32 v44, v23, v19
	v_mul_f32_e32 v45, v23, v20
	v_mul_f32_e32 v46, v23, v21
	s_waitcnt vmcnt(2)
	v_mul_f32_e32 v47, v23, v14
	v_mul_f32_e32 v48, v23, v15
	v_mul_f32_e32 v49, v23, v16
	v_mul_f32_e32 v50, v23, v17
	s_waitcnt vmcnt(1)
	v_mul_f32_e32 v51, v23, v6
	v_mul_f32_e32 v52, v23, v7
	v_mul_f32_e32 v53, v23, v8
	v_mul_f32_e32 v54, v23, v9
	s_waitcnt vmcnt(0)
	v_mul_f32_e32 v55, v23, v2
	v_mul_f32_e32 v56, v23, v3
	v_mul_f32_e32 v57, v23, v4
	v_mul_f32_e32 v58, v23, v5
	v_bfe_u32 v59, v39, 16, 1
	v_bfe_u32 v60, v40, 16, 1
	v_bfe_u32 v61, v41, 16, 1
	v_bfe_u32 v62, v42, 16, 1
	v_bfe_u32 v63, v43, 16, 1
	v_bfe_u32 v64, v44, 16, 1
	v_bfe_u32 v65, v45, 16, 1
	v_bfe_u32 v66, v46, 16, 1
	v_bfe_u32 v67, v47, 16, 1
	v_bfe_u32 v68, v48, 16, 1
	v_bfe_u32 v69, v49, 16, 1
	v_bfe_u32 v70, v50, 16, 1
	v_bfe_u32 v71, v51, 16, 1
	v_bfe_u32 v72, v52, 16, 1
	v_bfe_u32 v73, v53, 16, 1
	v_bfe_u32 v74, v54, 16, 1
	v_bfe_u32 v75, v55, 16, 1
	v_bfe_u32 v76, v56, 16, 1
	v_bfe_u32 v77, v57, 16, 1
	v_bfe_u32 v78, v58, 16, 1
	v_add3_u32 v39, v39, v59, s12
	v_add3_u32 v40, v40, v60, s12
	v_add3_u32 v41, v41, v61, s12
	v_add3_u32 v42, v42, v62, s12
	v_add3_u32 v43, v43, v63, s12
	v_add3_u32 v44, v44, v64, s12
	v_add3_u32 v45, v45, v65, s12
	v_add3_u32 v46, v46, v66, s12
	v_add3_u32 v47, v47, v67, s12
	v_add3_u32 v48, v48, v68, s12
	v_add3_u32 v49, v49, v69, s12
	v_add3_u32 v50, v50, v70, s12
	v_add3_u32 v51, v51, v71, s12
	v_add3_u32 v52, v52, v72, s12
	v_add3_u32 v53, v53, v73, s12
	v_add3_u32 v54, v54, v74, s12
	v_add3_u32 v55, v55, v75, s12
	v_add3_u32 v56, v56, v76, s12
	v_add3_u32 v57, v57, v77, s12
	v_add3_u32 v58, v58, v78, s12
	v_and_b32_e32 v59, 0xffff0000, v39
	ds_write_b16_d16_hi v30, v39
	v_and_b32_e32 v39, 0xffff0000, v40
	ds_write_b16_d16_hi v100, v40 offset:2048
	v_and_b32_e32 v40, 0xffff0000, v41
	ds_write_b16_d16_hi v101, v41 offset:4096
	v_and_b32_e32 v41, 0xffff0000, v42
	ds_write_b16_d16_hi v102, v42 offset:6144
	v_and_b32_e32 v42, 0xffff0000, v43
	ds_write_b16_d16_hi v103, v43 offset:8192
	v_and_b32_e32 v43, 0xffff0000, v44
	ds_write_b16_d16_hi v104, v44 offset:10240
	v_and_b32_e32 v44, 0xffff0000, v45
	ds_write_b16_d16_hi v105, v45 offset:12288
	v_and_b32_e32 v45, 0xffff0000, v46
	ds_write_b16_d16_hi v106, v46 offset:14336
	v_and_b32_e32 v46, 0xffff0000, v47
	ds_write_b16_d16_hi v107, v47 offset:16384
	v_and_b32_e32 v47, 0xffff0000, v48
	ds_write_b16_d16_hi v108, v48 offset:18432
	v_and_b32_e32 v48, 0xffff0000, v49
	ds_write_b16_d16_hi v109, v49 offset:20480
	v_and_b32_e32 v49, 0xffff0000, v50
	ds_write_b16_d16_hi v110, v50 offset:22528
	v_and_b32_e32 v50, 0xffff0000, v51
	ds_write_b16_d16_hi v111, v51 offset:24576
	v_and_b32_e32 v51, 0xffff0000, v52
	ds_write_b16_d16_hi v112, v52 offset:26624
	v_and_b32_e32 v52, 0xffff0000, v53
	ds_write_b16_d16_hi v113, v53 offset:28672
	v_and_b32_e32 v53, 0xffff0000, v54
	ds_write_b16_d16_hi v114, v54 offset:30720
	v_and_b32_e32 v54, 0xffff0000, v55
	ds_write_b16_d16_hi v30, v55 offset:32768
	v_and_b32_e32 v55, 0xffff0000, v56
	ds_write_b16_d16_hi v100, v56 offset:34816
	v_and_b32_e32 v56, 0xffff0000, v57
	ds_write_b16_d16_hi v101, v57 offset:36864
	v_and_b32_e32 v57, 0xffff0000, v58
	v_fma_f32 v10, v23, v10, -v59
	v_fma_f32 v11, v23, v11, -v39
	v_fma_f32 v12, v23, v12, -v40
	v_fma_f32 v13, v23, v13, -v41
	v_fma_f32 v18, v23, v18, -v42
	v_fma_f32 v19, v23, v19, -v43
	v_fma_f32 v20, v23, v20, -v44
	v_fma_f32 v21, v23, v21, -v45
	v_fma_f32 v14, v23, v14, -v46
	v_fma_f32 v15, v23, v15, -v47
	v_fma_f32 v16, v23, v16, -v48
	v_fma_f32 v17, v23, v17, -v49
	v_fma_f32 v6, v23, v6, -v50
	v_fma_f32 v7, v23, v7, -v51
	v_fma_f32 v8, v23, v8, -v52
	v_fma_f32 v9, v23, v9, -v53
	v_fma_f32 v2, v23, v2, -v54
	v_fma_f32 v3, v23, v3, -v55
	v_fma_f32 v4, v23, v4, -v56
	v_fma_f32 v5, v23, v5, -v57
	v_bfe_u32 v23, v10, 16, 1
	v_bfe_u32 v39, v11, 16, 1
	v_bfe_u32 v40, v12, 16, 1
	v_bfe_u32 v41, v13, 16, 1
	v_bfe_u32 v42, v18, 16, 1
	v_bfe_u32 v43, v19, 16, 1
	v_bfe_u32 v44, v20, 16, 1
	v_bfe_u32 v45, v21, 16, 1
	v_bfe_u32 v46, v14, 16, 1
	v_bfe_u32 v47, v15, 16, 1
	v_bfe_u32 v48, v16, 16, 1
	v_bfe_u32 v49, v17, 16, 1
	v_bfe_u32 v50, v6, 16, 1
	v_bfe_u32 v51, v7, 16, 1
	v_bfe_u32 v52, v8, 16, 1
	v_bfe_u32 v53, v9, 16, 1
	v_bfe_u32 v54, v2, 16, 1
	v_bfe_u32 v55, v3, 16, 1
	v_bfe_u32 v56, v4, 16, 1
	v_bfe_u32 v57, v5, 16, 1
	v_add3_u32 v10, v10, v23, s12
	ds_write_b16_d16_hi v102, v58 offset:38912
	v_add3_u32 v11, v11, v39, s12
	v_add3_u32 v12, v12, v40, s12
	v_add3_u32 v13, v13, v41, s12
	v_add3_u32 v18, v18, v42, s12
	v_add3_u32 v19, v19, v43, s12
	v_add3_u32 v20, v20, v44, s12
	v_add3_u32 v21, v21, v45, s12
	v_add3_u32 v14, v14, v46, s12
	v_add3_u32 v15, v15, v47, s12
	v_add3_u32 v16, v16, v48, s12
	v_add3_u32 v17, v17, v49, s12
	v_add3_u32 v6, v6, v50, s12
	v_add3_u32 v7, v7, v51, s12
	v_add3_u32 v8, v8, v52, s12
	v_add3_u32 v9, v9, v53, s12
	v_add3_u32 v2, v2, v54, s12
	v_add3_u32 v3, v3, v55, s12
	v_add3_u32 v4, v4, v56, s12
	v_add3_u32 v5, v5, v57, s12
	ds_write_b16_d16_hi v30, v10 offset:40960
	ds_write_b16_d16_hi v100, v11 offset:43008
	ds_write_b16_d16_hi v101, v12 offset:45056
	ds_write_b16_d16_hi v102, v13 offset:47104
	ds_write_b16_d16_hi v103, v18 offset:49152
	ds_write_b16_d16_hi v104, v19 offset:51200
	ds_write_b16_d16_hi v105, v20 offset:53248
	ds_write_b16_d16_hi v106, v21 offset:55296
	ds_write_b16_d16_hi v107, v14 offset:57344
	ds_write_b16_d16_hi v108, v15 offset:59392
	ds_write_b16_d16_hi v109, v16 offset:61440
	ds_write_b16_d16_hi v110, v17 offset:63488
	ds_write_b16_d16_hi v31, v6
	ds_write_b16_d16_hi v32, v7
	ds_write_b16_d16_hi v33, v8
	ds_write_b16_d16_hi v34, v9
	ds_write_b16_d16_hi v35, v2
	ds_write_b16_d16_hi v36, v3
	ds_write_b16_d16_hi v37, v4
	ds_write_b16_d16_hi v38, v5
	v_add_u32_e32 v30, 0x400, v30
	s_andn2_b64 exec, exec, s[4:5]
	s_cbranch_execnz .LBB0_899
	s_or_b64 exec, exec, s[4:5]
	v_cmp_gt_u32_e64 s[6:7], 24, v0
	s_and_saveexec_b64 s[4:5], s[6:7]
	v_lshl_add_u32 v1, v0, 2, 0
	v_add_u32_e32 v1, 0x1ed80, v1
	v_mov_b32_e32 v2, 0
	ds_write_b32 v1, v2
	s_or_b64 exec, exec, s[4:5]
	s_movk_i32 s4, 0x50
	v_cmp_gt_u32_e64 s[4:5], s4, v0
	s_and_saveexec_b64 s[8:9], s[4:5]
	v_lshl_add_u32 v1, v0, 2, 0
	v_add_u32_e32 v1, 0x1ee80, v1
	v_mov_b32_e32 v2, -1
	ds_write_b32 v1, v2
	s_or_b64 exec, exec, s[8:9]
	v_add_u32_e32 v1, 0xffffff80, v0
	v_cmp_gt_u32_e32 vcc, 20, v1
	s_and_saveexec_b64 s[8:9], vcc
	s_cbranch_execz .LBB0_906
	v_lshlrev_b32_e32 v2, 2, v0
	v_mov_b32_e32 v3, 0
	s_movk_i32 s10, 0xfe00
	v_lshl_add_u64 v[4:5], s[40:41], 0, v[2:3]
	s_mov_b32 s11, -1
	v_lshl_add_u64 v[4:5], v[4:5], 0, s[10:11]
	s_movk_i32 s10, 0xfdf0
	s_movk_i32 s12, 0x84
	v_lshl_add_u64 v[2:3], s[44:45], 0, v[2:3]
	s_mov_b32 s11, -1
	v_lshl_add_u64 v[2:3], v[2:3], 0, s[10:11]
	v_cmp_gt_u32_e32 vcc, s12, v0
	s_add_i32 s10, 0, 0x1f100
	s_nop 0
	v_cndmask_b32_e32 v3, v3, v5, vcc
	v_cndmask_b32_e32 v2, v2, v4, vcc
	global_load_dword v1, v[2:3], off
	v_lshl_add_u32 v2, v0, 2, s10
	v_add_u32_e32 v2, 0xfffffe00, v2
	s_waitcnt vmcnt(0)
	ds_write_b32 v2, v1
.LBB0_906:
	s_or_b64 exec, exec, s[8:9]
	s_lshl_b32 s14, s95, 6
	v_or_b32_e32 v2, s14, v222
	v_ashrrev_i32_e32 v3, 31, v2
	v_lshlrev_b64 v[2:3], 11, v[2:3]
	v_and_b32_e32 v1, 48, v0
	v_lshl_add_u64 v[2:3], s[82:83], 0, v[2:3]
	v_lshl_or_b32 v18, s92, 8, v1
	v_mov_b32_e32 v19, 0
	v_lshl_add_u64 v[14:15], v[2:3], 0, v[18:19]
	s_waitcnt lgkmcnt(0)
	s_barrier
	global_load_dwordx4 v[2:5], v[14:15], off offset:192
	global_load_dwordx4 v[6:9], v[14:15], off offset:128
	global_load_dwordx4 v[10:13], v[14:15], off
	s_nop 0
	global_load_dwordx4 v[14:17], v[14:15], off offset:64
	v_mbcnt_hi_u32_b32 v20, -1, v227
	v_and_b32_e32 v25, 64, v20
	v_and_b32_e32 v36, 0x3f0, v22
	v_xor_b32_e32 v22, 16, v20
	v_lshl_add_u64 v[34:35], s[82:83], 0, v[18:19]
	v_add_u32_e32 v19, 64, v25
	v_lshrrev_b32_e32 v21, 8, v0
	v_bfe_u32 v23, v0, 2, 4
	s_cmp_eq_u32 s95, 0
	v_xor_b32_e32 v26, 32, v20
	v_cmp_lt_i32_e32 vcc, v22, v19
	v_and_b32_e32 v1, 3, v0
	v_or_b32_e32 v24, 16, v222
	v_lshl_or_b32 v23, v21, 4, v23
	v_lshlrev_b32_e32 v39, 10, v21
	s_cselect_b32 s17, 5, 4
	s_and_b32 s12, s87, 0xffffffc0
	s_add_i32 s13, 0, 0x14000
	v_cndmask_b32_e32 v21, v20, v22, vcc
	v_cmp_lt_i32_e32 vcc, v26, v19
	v_and_or_b32 v38, v226, 12, v1
	v_min_u32_e32 v24, 19, v24
	v_add_u32_e32 v18, 0, v18
	s_add_i32 s19, 0, 0x1c400
	v_cndmask_b32_e32 v19, v20, v26, vcc
	s_add_i32 s12, s13, s12
	s_mov_b32 s15, 0
	v_cmp_gt_u32_e64 s[8:9], 16, v208
	v_mov_b32_e32 v37, 0x358637bd
	s_mov_b32 s16, 0x800000
	s_lshl_b32 s18, s92, 11
	v_cmp_eq_u32_e64 s[10:11], 0, v23
	v_lshl_add_u32 v40, v38, 2, s13
	v_lshl_add_u32 v41, v23, 2, s19
	v_lshl_add_u32 v42, v222, 11, v18
	v_and_b32_e32 v120, 15, v222
	v_lshlrev_b32_e32 v120, 4, v120
	v_xor_b32_e32 v120, v42, v120
	v_xor_b32_e32 v121, 64, v120
	v_xor_b32_e32 v122, 0x80, v120
	v_xor_b32_e32 v123, 0xc0, v120
	v_lshl_add_u32 v43, v24, 11, v18
	v_and_b32_e32 v124, 15, v24
	v_lshlrev_b32_e32 v124, 4, v124
	v_xor_b32_e32 v124, v43, v124
	v_xor_b32_e32 v125, 64, v124
	v_xor_b32_e32 v126, 0x80, v124
	v_xor_b32_e32 v127, 0xc0, v124
	v_lshlrev_b32_e32 v44, 2, v21
	v_lshlrev_b32_e32 v45, 2, v19
	v_lshl_add_u32 v46, v208, 2, s12
	s_waitcnt vmcnt(3)
	v_mov_b32_e32 v50, v2
	v_mov_b32_e32 v49, v3
	v_mov_b32_e32 v48, v4
	v_mov_b32_e32 v47, v5
	s_branch .LBB0_908

.LBB0_914:
	s_or_b64 exec, exec, s[12:13]
	s_waitcnt lgkmcnt(0)
	ds_read_b128 v[48:51], v120
	ds_read_b128 v[52:55], v121
	ds_read_b128 v[56:59], v120 offset:40960
	ds_read_b128 v[60:63], v121 offset:40960
	s_and_b32 s12, s15, 1
	s_lshl_b32 s13, s12, 14
	s_waitcnt lgkmcnt(3)
	v_mfma_f32_16x16x32_bf16 v[48:51], v[10:13], v[48:51], 0
	s_add_i32 s13, s13, 0
	s_add_i32 s13, s13, 0x14400
	s_add_i32 s20, s13, s18
	s_waitcnt lgkmcnt(1)
	v_mfma_f32_16x16x32_bf16 v[48:51], v[10:13], v[56:59], v[48:51]
	ds_read_b128 v[56:59], v124
	ds_read_b128 v[64:67], v125
	ds_read_b128 v[68:71], v124 offset:40960
	ds_read_b128 v[72:75], v125 offset:40960
	s_waitcnt lgkmcnt(3)
	v_mfma_f32_16x16x32_bf16 v[56:59], v[10:13], v[56:59], 0
	s_waitcnt lgkmcnt(1)
	v_mfma_f32_16x16x32_bf16 v[10:13], v[10:13], v[68:71], v[56:59]
	v_mfma_f32_16x16x32_bf16 v[48:51], v[14:17], v[52:55], v[48:51]
	v_mfma_f32_16x16x32_bf16 v[10:13], v[14:17], v[64:67], v[10:13]
	v_mfma_f32_16x16x32_bf16 v[48:51], v[14:17], v[60:63], v[48:51]
	s_waitcnt lgkmcnt(0)
	v_mfma_f32_16x16x32_bf16 v[10:13], v[14:17], v[72:75], v[10:13]
	ds_read_b128 v[14:17], v122
	ds_read_b128 v[52:55], v123
	s_waitcnt lgkmcnt(1)
	v_mfma_f32_16x16x32_bf16 v[14:17], v[6:9], v[14:17], v[48:51]
	s_nop 2
	ds_read_b128 v[48:51], v122 offset:40960
	ds_read_b128 v[56:59], v123 offset:40960
	s_waitcnt lgkmcnt(1)
	v_mfma_f32_16x16x32_bf16 v[14:17], v[6:9], v[48:51], v[14:17]
	ds_read_b128 v[48:51], v126
	ds_read_b128 v[60:63], v127
	s_waitcnt lgkmcnt(1)
	v_mfma_f32_16x16x32_bf16 v[10:13], v[6:9], v[48:51], v[10:13]
	ds_read_b128 v[48:51], v126 offset:40960
	ds_read_b128 v[64:67], v127 offset:40960
	s_waitcnt lgkmcnt(1)
	v_mfma_f32_16x16x32_bf16 v[6:9], v[6:9], v[48:51], v[10:13]
	v_mfma_f32_16x16x32_bf16 v[10:13], v[2:5], v[52:55], v[14:17]
	v_mfma_f32_16x16x32_bf16 v[6:9], v[2:5], v[60:63], v[6:9]
	s_nop 1
	v_lshl_add_u32 v14, v208, 4, s20
	v_mfma_f32_16x16x32_bf16 v[10:13], v[2:5], v[56:59], v[10:13]
	s_waitcnt lgkmcnt(0)
	v_mfma_f32_16x16x32_bf16 v[2:5], v[2:5], v[64:67], v[6:9]
	s_nop 5
	ds_write_b128 v14, v[10:13]
	s_nop 0
	ds_write_b128 v14, v[2:5] offset:1024
	v_lshl_add_u32 v2, v1, 2, s13
	s_waitcnt lgkmcnt(0)
	s_barrier
	v_add3_u32 v10, v2, v39, v36
	v_lshl_add_u32 v11, s12, 9, v40
	ds_read2st64_b32 v[2:3], v10 offset1:8
	ds_read2_b32 v[4:5], v11 offset1:16
	ds_read2st64_b32 v[6:7], v10 offset0:16 offset1:24
	ds_read2_b32 v[8:9], v11 offset0:32 offset1:48
	s_waitcnt lgkmcnt(3)
	v_add_f32_e32 v2, 0, v2
	s_waitcnt lgkmcnt(2)
	v_add_f32_e32 v4, 0, v4
	v_add_f32_e32 v2, v2, v3
	v_add_f32_e32 v3, v4, v5
	s_waitcnt lgkmcnt(1)
	v_add_f32_e32 v6, v2, v6
	s_waitcnt lgkmcnt(0)
	v_add_f32_e32 v8, v3, v8
	ds_read2st64_b32 v[2:3], v10 offset0:32 offset1:40
	ds_read2_b32 v[4:5], v11 offset0:64 offset1:80
	v_add_f32_e32 v12, v6, v7
	ds_read2_b32 v[6:7], v11 offset0:96 offset1:112
	v_add_f32_e32 v8, v8, v9
	s_waitcnt lgkmcnt(2)
	v_add_f32_e32 v2, v12, v2
	s_waitcnt lgkmcnt(1)
	v_add_f32_e32 v4, v8, v4
	v_add_f32_e32 v8, v4, v5
	s_waitcnt lgkmcnt(0)
	v_add_f32_e32 v6, v8, v6
	v_add_f32_e32 v6, v6, v7
	v_fmamk_f32 v6, v6, 0x3a800000, v37
	ds_read2st64_b32 v[4:5], v10 offset0:48 offset1:56
	v_mul_f32_e32 v7, 0x4b800000, v6
	v_cmp_gt_f32_e32 vcc, s16, v6
	v_add_f32_e32 v2, v2, v3
	s_waitcnt lgkmcnt(0)
	v_add_f32_e32 v2, v2, v4
	v_cndmask_b32_e32 v6, v6, v7, vcc
	v_rsq_f32_e32 v6, v6
	v_add_f32_e32 v3, v2, v5
	v_mul_f32_e32 v2, 0x45800000, v6
	v_cndmask_b32_e32 v2, v6, v2, vcc
	v_mul_f32_e32 v4, v3, v2
	v_lshl_or_b32 v3, s15, 4, v38
	v_lshl_add_u32 v5, v3, 7, v41
	ds_write_b32 v5, v4
	s_and_saveexec_b64 s[12:13], s[10:11]
	s_cbranch_execz .LBB0_907
	v_lshl_add_u32 v3, v3, 2, 0
	v_add_u32_e32 v3, 0x1ec00, v3
	ds_write_b32 v3, v2
	s_branch .LBB0_907
